# row-count read for the MFMA skip flags joins the unit decode LDS round trip
# baseline (speedup 1.0000x reference)
;     __device__ __forceinline__ bool next(int i, pg8::Unit& u) const {
;         const int NB = __builtin_amdgcn_readfirstlane(tab[0]); const int L = i * G + c; if (L >= NB * nN) return false;
;         const int b = L / nN, pn = L - b * nN, e = __builtin_amdgcn_readfirstlane(tab[64 + b]);
;         u.pa = A; u.pb = B + (size_t)e * bexp + (size_t)pn * 256 * 128; u.row0 = b * 256; u.col0 = pn * 256; u.aux = e; u.blk = b; return true;
;     }
.LBB0_923:
	s_lshr_b32 s99, s73, 6
	s_add_i32 s99, s99, 0x22400
	v_mov_b32_e32 v250, s99
	ds_read_b32 v250, v250
	s_lshr_b32 s101, s93, 2
	s_lshl_b32 s101, s101, 6
	ds_read_b32 v2, v213
	s_add_i32 s71, s46, 1
	s_lshl_b32 s2, s71, 2
	s_add_i32 s2, s2, 0x23c00
	v_mov_b32_e32 v249, s2
	ds_read_b32 v249, v249
	s_waitcnt lgkmcnt(0)
	v_readfirstlane_b32 s99, v250
	s_cmp_le_i32 s99, s101
	s_cselect_b32 s100, 1, 0
	s_add_i32 s101, s101, 0x80
	s_cmp_le_i32 s99, s101
	s_cselect_b32 s99, 2, 0
	s_or_b32 s99, s99, s100
	v_readfirstlane_b32 s3, v2
	s_lshl_b32 s3, s3, 4
	v_readfirstlane_b32 s2, v249
	s_cmp_lt_i32 s2, s3
	s_cselect_b64 s[40:41], -1, 0
	s_cmp_ge_i32 s2, s3
	s_cbranch_scc1 .LBB0_925
	s_ashr_i32 s3, s2, 31
	s_lshr_b32 s3, s3, 28
	s_add_i32 s3, s2, s3
	s_ashr_i32 s70, s3, 4
	s_lshl_b32 s26, s70, 2
	s_add_i32 s26, s26, 0
	s_add_i32 s26, s26, 0x22100
	v_mov_b32_e32 v2, s26
	ds_read_b32 v2, v2
	s_and_b32 s3, s3, -16
	s_sub_i32 s2, s2, s3
	s_waitcnt lgkmcnt(0)
	v_readfirstlane_b32 s26, v2
	s_ashr_i32 s27, s26, 31
	s_lshl_b64 s[28:29], s[26:27], 23
	s_add_u32 s27, s25, s28
	s_addc_u32 s30, s33, s29
	s_ashr_i32 s3, s2, 31
	s_lshl_b64 s[28:29], s[2:3], 15
	s_add_u32 s28, s27, s28
	s_addc_u32 s29, s30, s29
	s_lshl_b32 s72, s70, 8
	s_lshl_b32 s27, s2, 8

;     __device__ __forceinline__ bool next(int i, pg8::Unit& u) const {
;         const int NB = __builtin_amdgcn_readfirstlane(tab[0]); const int L = i * G + c; if (L >= NB * nN) return false;
;         const int b = L / nN, pn = L - b * nN, e = __builtin_amdgcn_readfirstlane(tab[64 + b]);
;         u.pa = A; u.pb = B + (size_t)e * bexp + (size_t)pn * 256 * 128; u.row0 = b * 256; u.col0 = pn * 256; u.aux = e; u.blk = b; return true;
;     }
.LBB0_1028:
	s_lshr_b32 s99, s69, 6
	s_add_i32 s99, s99, 0x22400
	v_mov_b32_e32 v250, s99
	ds_read_b32 v250, v250
	s_lshr_b32 s101, s93, 2
	s_lshl_b32 s101, s101, 6
	ds_read_b32 v2, v221
	s_add_i32 s67, s38, 1
	s_lshl_b32 s31, s67, 2
	s_add_i32 s31, s31, 0x23c00
	v_mov_b32_e32 v249, s31
	ds_read_b32 v249, v249
	s_waitcnt lgkmcnt(0)
	v_readfirstlane_b32 s99, v250
	s_cmp_le_i32 s99, s101
	s_cselect_b32 s100, 1, 0
	s_add_i32 s101, s101, 0x80
	s_cmp_le_i32 s99, s101
	s_cselect_b32 s99, 2, 0
	s_or_b32 s99, s99, s100
	v_readfirstlane_b32 s28, v2
	s_lshl_b32 s35, s28, 3
	v_readfirstlane_b32 s31, v249
	s_cmp_lt_i32 s31, s35
	s_cselect_b64 s[28:29], -1, 0
	s_cmp_ge_i32 s31, s35
	s_cbranch_scc1 .LBB0_1030
	s_ashr_i32 s24, s31, 31
	s_lshr_b32 s24, s24, 29
	s_add_i32 s24, s31, s24
	s_ashr_i32 s35, s24, 3
	s_lshl_b32 s25, s35, 2
	s_add_i32 s25, s25, 0
	s_add_i32 s25, s25, 0x22100
	v_mov_b32_e32 v2, s25
	ds_read_b32 v2, v2
	s_and_b32 s24, s24, -8
	s_sub_i32 s40, s31, s24
	s_waitcnt lgkmcnt(0)
	v_readfirstlane_b32 s24, v2
	s_ashr_i32 s25, s24, 31
	s_lshl_b64 s[26:27], s[24:25], 22
	s_add_u32 s25, s23, s26
	s_addc_u32 s31, s33, s27
	s_ashr_i32 s41, s40, 31
	s_lshl_b64 s[26:27], s[40:41], 15
	s_add_u32 s26, s25, s26
	s_addc_u32 s27, s31, s27
	s_lshl_b32 s68, s35, 8
	s_lshl_b32 s25, s40, 8
